# speedup vs baseline: 1.1027x; 1.0086x over previous
_Z11center_mainPKfPKcS0_Pf:
	s_load_dwordx4 s[4:7], s[0:1], 0x0
	s_load_dwordx2 s[8:9], s[0:1], 0x10
	s_and_b32 s3, s2, 7
	s_lshr_b32 s12, s2, 3
	s_mov_b32 s30, s2
	v_lshrrev_b32_e32 v1, 6, v0
	v_and_b32_e32 v2, 63, v0
	v_bfe_u32 v3, v0, 3, 3
	v_and_b32_e32 v4, 7, v0
	v_lshrrev_b32_e32 v5, 7, v0
	v_bfe_u32 v6, v0, 6, 1
	v_lshl_or_b32 v7, v5, 3, v3
	v_lshlrev_b32_e32 v8, 10, v7
	v_lshl_or_b32 v8, v6, 9, v8
	v_lshl_or_b32 v226, v4, 4, v8
	v_lshlrev_b32_e32 v17, 15, v1
	v_lshl_or_b32 v227, v2, 5, v17
	v_lshlrev_b32_e32 v237, 3, v0
	s_lshl_b32 s13, s3, 22
	s_lshl_b32 s14, s12, 15
	s_add_u32 s13, s13, s14
	s_lshl_b32 s15, s3, 18
	s_lshl_b32 s28, s3, 12
	s_waitcnt lgkmcnt(0)
	s_add_u32 s16, s4, s13
	s_addc_u32 s17, s5, 0
	s_add_u32 s18, s16, 0x100000
	s_addc_u32 s19, s17, 0
	s_add_u32 s20, s16, 0x200000
	s_addc_u32 s21, s17, 0
	s_add_u32 s22, s16, 0x300000
	s_addc_u32 s23, s17, 0
	s_add_u32 s24, s6, s15
	s_addc_u32 s25, s7, 0
	s_add_u32 s8, s8, s28
	s_addc_u32 s9, s9, 0
	s_add_u32 s32, s24, 0x1000
	s_addc_u32 s33, s25, 0
	s_add_u32 s34, s24, 0x2000
	s_addc_u32 s35, s25, 0
	s_add_u32 s36, s24, 0x3000
	s_addc_u32 s37, s25, 0
	s_add_u32 s38, s24, 0x4000
	s_addc_u32 s39, s25, 0
	s_add_u32 s40, s24, 0x5000
	s_addc_u32 s41, s25, 0
	s_add_u32 s42, s24, 0x6000
	s_addc_u32 s43, s25, 0
	s_add_u32 s44, s24, 0x7000
	s_addc_u32 s45, s25, 0
	global_load_dwordx2 v[238:239], v237, s[8:9]
	global_load_dwordx4 v[194:197], v226, s[16:17] offset:0 nt
	global_load_dwordx4 v[198:201], v226, s[16:17] offset:128 nt
	global_load_dwordx4 v[202:205], v226, s[16:17] offset:256 nt
	global_load_dwordx4 v[206:209], v226, s[16:17] offset:384 nt
	global_load_dwordx4 v[34:37], v227, s[24:25] offset:0
	global_load_dwordx4 v[38:41], v227, s[24:25] offset:16
	global_load_dwordx4 v[26:29], v227, s[24:25] offset:2048
	global_load_dwordx4 v[30:33], v227, s[24:25] offset:2064
	global_load_dwordx4 v[50:53], v227, s[32:33] offset:0
	global_load_dwordx4 v[54:57], v227, s[32:33] offset:16
	global_load_dwordx4 v[42:45], v227, s[32:33] offset:2048
	global_load_dwordx4 v[46:49], v227, s[32:33] offset:2064
	global_load_dwordx4 v[18:21], v227, s[34:35] offset:0
	global_load_dwordx4 v[22:25], v227, s[34:35] offset:16
	global_load_dwordx4 v[130:133], v227, s[34:35] offset:2048
	global_load_dwordx4 v[134:137], v227, s[34:35] offset:2064
	global_load_dwordx4 v[122:125], v227, s[36:37] offset:0
	global_load_dwordx4 v[126:129], v227, s[36:37] offset:16
	global_load_dwordx4 v[138:141], v227, s[36:37] offset:2048
	global_load_dwordx4 v[142:145], v227, s[36:37] offset:2064
	global_load_dwordx4 v[98:101], v227, s[38:39] offset:0
	global_load_dwordx4 v[102:105], v227, s[38:39] offset:16
	global_load_dwordx4 v[90:93], v227, s[38:39] offset:2048
	global_load_dwordx4 v[94:97], v227, s[38:39] offset:2064
	global_load_dwordx4 v[114:117], v227, s[40:41] offset:0
	global_load_dwordx4 v[118:121], v227, s[40:41] offset:16
	global_load_dwordx4 v[106:109], v227, s[40:41] offset:2048
	global_load_dwordx4 v[110:113], v227, s[40:41] offset:2064
	global_load_dwordx4 v[58:61], v227, s[42:43] offset:0
	global_load_dwordx4 v[62:65], v227, s[42:43] offset:16
	global_load_dwordx4 v[66:69], v227, s[42:43] offset:2048
	global_load_dwordx4 v[70:73], v227, s[42:43] offset:2064
	global_load_dwordx4 v[74:77], v227, s[44:45] offset:0
	global_load_dwordx4 v[78:81], v227, s[44:45] offset:16
	global_load_dwordx4 v[82:85], v227, s[44:45] offset:2048
	global_load_dwordx4 v[86:89], v227, s[44:45] offset:2064
	v_mul_u32_u24_e32 v9, 0x110, v7
	v_lshl_add_u32 v9, v6, 7, v9
	v_lshl_add_u32 v228, v4, 4, v9
	v_lshlrev_b32_e32 v10, 6, v7
	v_lshl_or_b32 v10, v6, 5, v10
	v_lshl_or_b32 v229, v4, 2, v10
	v_and_b32_e32 v11, 31, v0
	v_bfe_u32 v12, v0, 5, 1
	v_mul_u32_u24_e32 v13, 0x110, v11
	v_lshl_add_u32 v230, v12, 5, v13
	v_lshlrev_b32_e32 v14, 9, v1
	v_lshl_or_b32 v231, v12, 4, v14
	v_xor_b32_e32 v15, 32, v2
	v_lshlrev_b32_e32 v232, 2, v15
	v_lshlrev_b32_e32 v16, 7, v1
	v_lshl_or_b32 v233, v11, 2, v16
	v_mov_b32_e32 v234, 0x7f7f7f7f
	s_waitcnt vmcnt(32)
	ds_write_b64 v237, v[238:239] offset:34816
	v_mul_f32_e32 v244, v194, v194
	v_mul_f32_e32 v245, v198, v198
	v_cvt_pk_fp8_f32 v240, v194, v195
	v_cvt_pk_fp8_f32 v241, v198, v199
	v_cvt_pk_fp8_f32 v242, v202, v203
	v_cvt_pk_fp8_f32 v243, v206, v207
	v_fmac_f32_e32 v244, v195, v195
	v_fmac_f32_e32 v245, v199, v199
	v_fmac_f32_e32 v244, v196, v196
	v_fmac_f32_e32 v245, v200, v200
	v_fmac_f32_e32 v244, v197, v197
	v_fmac_f32_e32 v245, v201, v201
	v_fmac_f32_e32 v244, v202, v202
	v_fmac_f32_e32 v245, v206, v206
	v_fmac_f32_e32 v244, v203, v203
	v_fmac_f32_e32 v245, v207, v207
	v_fmac_f32_e32 v244, v204, v204
	v_fmac_f32_e32 v245, v208, v208
	v_fmac_f32_e32 v244, v205, v205
	v_fmac_f32_e32 v245, v209, v209
	v_cvt_pk_fp8_f32 v240, v196, v197 op_sel:[0,0,1]
	v_cvt_pk_fp8_f32 v241, v200, v201 op_sel:[0,0,1]
	v_cvt_pk_fp8_f32 v242, v204, v205 op_sel:[0,0,1]
	v_cvt_pk_fp8_f32 v243, v208, v209 op_sel:[0,0,1]
	v_add_f32_e32 v244, v244, v245
	s_nop 0
	ds_write_b128 v228, v[240:243] offset:0
	ds_write_b32 v229, v244 offset:38912
	global_load_dwordx4 v[210:213], v226, s[18:19] offset:0 nt
	global_load_dwordx4 v[214:217], v226, s[18:19] offset:128 nt
	global_load_dwordx4 v[218:221], v226, s[18:19] offset:256 nt
	global_load_dwordx4 v[222:225], v226, s[18:19] offset:384 nt
	s_waitcnt lgkmcnt(0)
	s_barrier
	ds_read_b128 v[162:165], v230 offset:0
	ds_read_b128 v[166:169], v230 offset:16
	ds_read_b128 v[2:5], v231 offset:34816
	ds_read_b128 v[6:9], v231 offset:34848
	ds_read_b128 v[10:13], v231 offset:34880
	ds_read_b128 v[14:17], v231 offset:34912
	ds_read_b128 v[170:173], v230 offset:64
	ds_read_b128 v[174:177], v230 offset:80
	ds_read_b128 v[178:181], v230 offset:128
	ds_read_b128 v[182:185], v230 offset:144
	ds_read_b128 v[186:189], v230 offset:192
	ds_read_b128 v[190:193], v230 offset:208
	s_waitcnt vmcnt(34) lgkmcnt(6)
	v_mfma_scale_f32_32x32x64_f8f6f4 v[2:17], v[34:41], v[162:169], v[2:17], v234, v234 op_sel_hi:[0,0,0]
	s_waitcnt vmcnt(32) lgkmcnt(4)
	v_mfma_scale_f32_32x32x64_f8f6f4 v[2:17], v[26:33], v[170:177], v[2:17], v234, v234 op_sel_hi:[0,0,0]
	s_waitcnt vmcnt(30) lgkmcnt(2)
	v_mfma_scale_f32_32x32x64_f8f6f4 v[2:17], v[50:57], v[178:185], v[2:17], v234, v234 op_sel_hi:[0,0,0]
	s_waitcnt vmcnt(28) lgkmcnt(0)
	v_mfma_scale_f32_32x32x64_f8f6f4 v[2:17], v[42:49], v[186:193], v[2:17], v234, v234 op_sel_hi:[0,0,0]
	ds_read_b128 v[146:149], v231 offset:34944
	ds_read_b128 v[150:153], v231 offset:34976
	ds_read_b128 v[154:157], v231 offset:35008
	ds_read_b128 v[158:161], v231 offset:35040
	s_waitcnt vmcnt(26) lgkmcnt(0)
	v_mfma_scale_f32_32x32x64_f8f6f4 v[146:161], v[18:25], v[162:169], v[146:161], v234, v234 op_sel_hi:[0,0,0]
	s_waitcnt vmcnt(24)
	v_mfma_scale_f32_32x32x64_f8f6f4 v[146:161], v[130:137], v[170:177], v[146:161], v234, v234 op_sel_hi:[0,0,0]
	s_waitcnt vmcnt(22)
	v_mfma_scale_f32_32x32x64_f8f6f4 v[146:161], v[122:129], v[178:185], v[146:161], v234, v234 op_sel_hi:[0,0,0]
	s_waitcnt vmcnt(20)
	v_mfma_scale_f32_32x32x64_f8f6f4 v[146:161], v[138:145], v[186:193], v[146:161], v234, v234 op_sel_hi:[0,0,0]
	s_nop 15
	v_min3_f32 v2, v2, v3, v4
	v_min3_f32 v5, v5, v6, v7
	v_min3_f32 v8, v8, v9, v10
	v_min3_f32 v11, v11, v12, v13
	v_min3_f32 v14, v14, v15, v16
	v_min3_f32 v2, v2, v5, v8
	v_min3_f32 v11, v11, v14, v17
	v_min_f32_e32 v235, v2, v11
	ds_read_b128 v[2:5], v231 offset:35072
	ds_read_b128 v[6:9], v231 offset:35104
	ds_read_b128 v[10:13], v231 offset:35136
	ds_read_b128 v[14:17], v231 offset:35168
	s_waitcnt vmcnt(18) lgkmcnt(0)
	v_mfma_scale_f32_32x32x64_f8f6f4 v[2:17], v[98:105], v[162:169], v[2:17], v234, v234 op_sel_hi:[0,0,0]
	s_waitcnt vmcnt(16)
	v_mfma_scale_f32_32x32x64_f8f6f4 v[2:17], v[90:97], v[170:177], v[2:17], v234, v234 op_sel_hi:[0,0,0]
	s_waitcnt vmcnt(14)
	v_mfma_scale_f32_32x32x64_f8f6f4 v[2:17], v[114:121], v[178:185], v[2:17], v234, v234 op_sel_hi:[0,0,0]
	s_waitcnt vmcnt(12)
	v_mfma_scale_f32_32x32x64_f8f6f4 v[2:17], v[106:113], v[186:193], v[2:17], v234, v234 op_sel_hi:[0,0,0]
	s_nop 15
	v_min3_f32 v146, v146, v147, v148
	v_min3_f32 v149, v149, v150, v151
	v_min3_f32 v152, v152, v153, v154
	v_min3_f32 v155, v155, v156, v157
	v_min3_f32 v158, v158, v159, v160
	v_min3_f32 v146, v146, v149, v152
	v_min3_f32 v155, v155, v158, v161
	v_min3_f32 v235, v235, v146, v155
	ds_read_b128 v[146:149], v231 offset:35200
	ds_read_b128 v[150:153], v231 offset:35232
	ds_read_b128 v[154:157], v231 offset:35264
	ds_read_b128 v[158:161], v231 offset:35296
	s_waitcnt vmcnt(10) lgkmcnt(0)
	v_mfma_scale_f32_32x32x64_f8f6f4 v[146:161], v[58:65], v[162:169], v[146:161], v234, v234 op_sel_hi:[0,0,0]
	s_waitcnt vmcnt(8)
	v_mfma_scale_f32_32x32x64_f8f6f4 v[146:161], v[66:73], v[170:177], v[146:161], v234, v234 op_sel_hi:[0,0,0]
	s_waitcnt vmcnt(6)
	v_mfma_scale_f32_32x32x64_f8f6f4 v[146:161], v[74:81], v[178:185], v[146:161], v234, v234 op_sel_hi:[0,0,0]
	s_waitcnt vmcnt(4)
	v_mfma_scale_f32_32x32x64_f8f6f4 v[146:161], v[82:89], v[186:193], v[146:161], v234, v234 op_sel_hi:[0,0,0]
	s_nop 15
	v_min3_f32 v2, v2, v3, v4
	v_min3_f32 v5, v5, v6, v7
	v_min3_f32 v8, v8, v9, v10
	v_min3_f32 v11, v11, v12, v13
	v_min3_f32 v14, v14, v15, v16
	v_min3_f32 v2, v2, v5, v8
	v_min3_f32 v11, v11, v14, v17
	v_min3_f32 v235, v235, v2, v11
	s_nop 15
	s_nop 3
	v_min3_f32 v146, v146, v147, v148
	v_min3_f32 v149, v149, v150, v151
	v_min3_f32 v152, v152, v153, v154
	v_min3_f32 v155, v155, v156, v157
	v_min3_f32 v158, v158, v159, v160
	v_min3_f32 v146, v146, v149, v152
	v_min3_f32 v155, v155, v158, v161
	v_min3_f32 v235, v235, v146, v155
	ds_bpermute_b32 v246, v232, v235
	s_waitcnt lgkmcnt(0)
	v_min_f32_e32 v246, v235, v246
	ds_write_b32 v233, v246 offset:47104
	global_load_dwordx4 v[194:197], v226, s[20:21] offset:0 nt
	global_load_dwordx4 v[198:201], v226, s[20:21] offset:128 nt
	global_load_dwordx4 v[202:205], v226, s[20:21] offset:256 nt
	global_load_dwordx4 v[206:209], v226, s[20:21] offset:384 nt
	s_waitcnt vmcnt(4)
	v_mul_f32_e32 v244, v210, v210
	v_mul_f32_e32 v245, v214, v214
	v_cvt_pk_fp8_f32 v240, v210, v211
	v_cvt_pk_fp8_f32 v241, v214, v215
	v_cvt_pk_fp8_f32 v242, v218, v219
	v_cvt_pk_fp8_f32 v243, v222, v223
	v_fmac_f32_e32 v244, v211, v211
	v_fmac_f32_e32 v245, v215, v215
	v_fmac_f32_e32 v244, v212, v212
	v_fmac_f32_e32 v245, v216, v216
	v_fmac_f32_e32 v244, v213, v213
	v_fmac_f32_e32 v245, v217, v217
	v_fmac_f32_e32 v244, v218, v218
	v_fmac_f32_e32 v245, v222, v222
	v_fmac_f32_e32 v244, v219, v219
	v_fmac_f32_e32 v245, v223, v223
	v_fmac_f32_e32 v244, v220, v220
	v_fmac_f32_e32 v245, v224, v224
	v_fmac_f32_e32 v244, v221, v221
	v_fmac_f32_e32 v245, v225, v225
	v_cvt_pk_fp8_f32 v240, v212, v213 op_sel:[0,0,1]
	v_cvt_pk_fp8_f32 v241, v216, v217 op_sel:[0,0,1]
	v_cvt_pk_fp8_f32 v242, v220, v221 op_sel:[0,0,1]
	v_cvt_pk_fp8_f32 v243, v224, v225 op_sel:[0,0,1]
	v_add_f32_e32 v244, v244, v245
	s_nop 0
	ds_write_b128 v228, v[240:243] offset:8704
	ds_write_b32 v229, v244 offset:40960
	s_waitcnt lgkmcnt(0)
	s_barrier
	ds_read_b128 v[162:165], v230 offset:8704
	ds_read_b128 v[166:169], v230 offset:8720
	ds_read_b128 v[2:5], v231 offset:34816
	ds_read_b128 v[6:9], v231 offset:34848
	ds_read_b128 v[10:13], v231 offset:34880
	ds_read_b128 v[14:17], v231 offset:34912
	ds_read_b128 v[170:173], v230 offset:8768
	ds_read_b128 v[174:177], v230 offset:8784
	ds_read_b128 v[178:181], v230 offset:8832
	ds_read_b128 v[182:185], v230 offset:8848
	ds_read_b128 v[186:189], v230 offset:8896
	ds_read_b128 v[190:193], v230 offset:8912
	s_waitcnt lgkmcnt(6)
	v_mfma_scale_f32_32x32x64_f8f6f4 v[2:17], v[34:41], v[162:169], v[2:17], v234, v234 op_sel_hi:[0,0,0]
	s_waitcnt lgkmcnt(4)
	v_mfma_scale_f32_32x32x64_f8f6f4 v[2:17], v[26:33], v[170:177], v[2:17], v234, v234 op_sel_hi:[0,0,0]
	s_waitcnt lgkmcnt(2)
	v_mfma_scale_f32_32x32x64_f8f6f4 v[2:17], v[50:57], v[178:185], v[2:17], v234, v234 op_sel_hi:[0,0,0]
	s_waitcnt lgkmcnt(0)
	v_mfma_scale_f32_32x32x64_f8f6f4 v[2:17], v[42:49], v[186:193], v[2:17], v234, v234 op_sel_hi:[0,0,0]
	ds_read_b128 v[146:149], v231 offset:34944
	ds_read_b128 v[150:153], v231 offset:34976
	ds_read_b128 v[154:157], v231 offset:35008
	ds_read_b128 v[158:161], v231 offset:35040
	s_waitcnt lgkmcnt(0)
	v_mfma_scale_f32_32x32x64_f8f6f4 v[146:161], v[18:25], v[162:169], v[146:161], v234, v234 op_sel_hi:[0,0,0]
	v_mfma_scale_f32_32x32x64_f8f6f4 v[146:161], v[130:137], v[170:177], v[146:161], v234, v234 op_sel_hi:[0,0,0]
	v_mfma_scale_f32_32x32x64_f8f6f4 v[146:161], v[122:129], v[178:185], v[146:161], v234, v234 op_sel_hi:[0,0,0]
	v_mfma_scale_f32_32x32x64_f8f6f4 v[146:161], v[138:145], v[186:193], v[146:161], v234, v234 op_sel_hi:[0,0,0]
	s_nop 15
	v_min3_f32 v2, v2, v3, v4
	v_min3_f32 v5, v5, v6, v7
	v_min3_f32 v8, v8, v9, v10
	v_min3_f32 v11, v11, v12, v13
	v_min3_f32 v14, v14, v15, v16
	v_min3_f32 v2, v2, v5, v8
	v_min3_f32 v11, v11, v14, v17
	v_min_f32_e32 v235, v2, v11
	ds_read_b128 v[2:5], v231 offset:35072
	ds_read_b128 v[6:9], v231 offset:35104
	ds_read_b128 v[10:13], v231 offset:35136
	ds_read_b128 v[14:17], v231 offset:35168
	s_waitcnt lgkmcnt(0)
	v_mfma_scale_f32_32x32x64_f8f6f4 v[2:17], v[98:105], v[162:169], v[2:17], v234, v234 op_sel_hi:[0,0,0]
	v_mfma_scale_f32_32x32x64_f8f6f4 v[2:17], v[90:97], v[170:177], v[2:17], v234, v234 op_sel_hi:[0,0,0]
	v_mfma_scale_f32_32x32x64_f8f6f4 v[2:17], v[114:121], v[178:185], v[2:17], v234, v234 op_sel_hi:[0,0,0]
	v_mfma_scale_f32_32x32x64_f8f6f4 v[2:17], v[106:113], v[186:193], v[2:17], v234, v234 op_sel_hi:[0,0,0]
	s_nop 15
	v_min3_f32 v146, v146, v147, v148
	v_min3_f32 v149, v149, v150, v151
	v_min3_f32 v152, v152, v153, v154
	v_min3_f32 v155, v155, v156, v157
	v_min3_f32 v158, v158, v159, v160
	v_min3_f32 v146, v146, v149, v152
	v_min3_f32 v155, v155, v158, v161
	v_min3_f32 v235, v235, v146, v155
	ds_read_b128 v[146:149], v231 offset:35200
	ds_read_b128 v[150:153], v231 offset:35232
	ds_read_b128 v[154:157], v231 offset:35264
	ds_read_b128 v[158:161], v231 offset:35296
	s_waitcnt lgkmcnt(0)
	v_mfma_scale_f32_32x32x64_f8f6f4 v[146:161], v[58:65], v[162:169], v[146:161], v234, v234 op_sel_hi:[0,0,0]
	v_mfma_scale_f32_32x32x64_f8f6f4 v[146:161], v[66:73], v[170:177], v[146:161], v234, v234 op_sel_hi:[0,0,0]
	v_mfma_scale_f32_32x32x64_f8f6f4 v[146:161], v[74:81], v[178:185], v[146:161], v234, v234 op_sel_hi:[0,0,0]
	v_mfma_scale_f32_32x32x64_f8f6f4 v[146:161], v[82:89], v[186:193], v[146:161], v234, v234 op_sel_hi:[0,0,0]
	s_nop 15
	v_min3_f32 v2, v2, v3, v4
	v_min3_f32 v5, v5, v6, v7
	v_min3_f32 v8, v8, v9, v10
	v_min3_f32 v11, v11, v12, v13
	v_min3_f32 v14, v14, v15, v16
	v_min3_f32 v2, v2, v5, v8
	v_min3_f32 v11, v11, v14, v17
	v_min3_f32 v235, v235, v2, v11
	s_nop 15
	s_nop 3
	v_min3_f32 v146, v146, v147, v148
	v_min3_f32 v149, v149, v150, v151
	v_min3_f32 v152, v152, v153, v154
	v_min3_f32 v155, v155, v156, v157
	v_min3_f32 v158, v158, v159, v160
	v_min3_f32 v146, v146, v149, v152
	v_min3_f32 v155, v155, v158, v161
	v_min3_f32 v235, v235, v146, v155
	ds_bpermute_b32 v246, v232, v235
	s_waitcnt lgkmcnt(0)
	v_min_f32_e32 v246, v235, v246
	ds_write_b32 v233, v246 offset:48128
	global_load_dwordx4 v[210:213], v226, s[22:23] offset:0 nt
	global_load_dwordx4 v[214:217], v226, s[22:23] offset:128 nt
	global_load_dwordx4 v[218:221], v226, s[22:23] offset:256 nt
	global_load_dwordx4 v[222:225], v226, s[22:23] offset:384 nt
	s_waitcnt vmcnt(4)
	v_mul_f32_e32 v244, v194, v194
	v_mul_f32_e32 v245, v198, v198
	v_cvt_pk_fp8_f32 v240, v194, v195
	v_cvt_pk_fp8_f32 v241, v198, v199
	v_cvt_pk_fp8_f32 v242, v202, v203
	v_cvt_pk_fp8_f32 v243, v206, v207
	v_fmac_f32_e32 v244, v195, v195
	v_fmac_f32_e32 v245, v199, v199
	v_fmac_f32_e32 v244, v196, v196
	v_fmac_f32_e32 v245, v200, v200
	v_fmac_f32_e32 v244, v197, v197
	v_fmac_f32_e32 v245, v201, v201
	v_fmac_f32_e32 v244, v202, v202
	v_fmac_f32_e32 v245, v206, v206
	v_fmac_f32_e32 v244, v203, v203
	v_fmac_f32_e32 v245, v207, v207
	v_fmac_f32_e32 v244, v204, v204
	v_fmac_f32_e32 v245, v208, v208
	v_fmac_f32_e32 v244, v205, v205
	v_fmac_f32_e32 v245, v209, v209
	v_cvt_pk_fp8_f32 v240, v196, v197 op_sel:[0,0,1]
	v_cvt_pk_fp8_f32 v241, v200, v201 op_sel:[0,0,1]
	v_cvt_pk_fp8_f32 v242, v204, v205 op_sel:[0,0,1]
	v_cvt_pk_fp8_f32 v243, v208, v209 op_sel:[0,0,1]
	v_add_f32_e32 v244, v244, v245
	s_nop 0
	ds_write_b128 v228, v[240:243] offset:17408
	ds_write_b32 v229, v244 offset:43008
	s_waitcnt lgkmcnt(0)
	s_barrier
	ds_read_b128 v[162:165], v230 offset:17408
	ds_read_b128 v[166:169], v230 offset:17424
	ds_read_b128 v[2:5], v231 offset:34816
	ds_read_b128 v[6:9], v231 offset:34848
	ds_read_b128 v[10:13], v231 offset:34880
	ds_read_b128 v[14:17], v231 offset:34912
	ds_read_b128 v[170:173], v230 offset:17472
	ds_read_b128 v[174:177], v230 offset:17488
	ds_read_b128 v[178:181], v230 offset:17536
	ds_read_b128 v[182:185], v230 offset:17552
	ds_read_b128 v[186:189], v230 offset:17600
	ds_read_b128 v[190:193], v230 offset:17616
	s_waitcnt lgkmcnt(6)
	v_mfma_scale_f32_32x32x64_f8f6f4 v[2:17], v[34:41], v[162:169], v[2:17], v234, v234 op_sel_hi:[0,0,0]
	s_waitcnt lgkmcnt(4)
	v_mfma_scale_f32_32x32x64_f8f6f4 v[2:17], v[26:33], v[170:177], v[2:17], v234, v234 op_sel_hi:[0,0,0]
	s_waitcnt lgkmcnt(2)
	v_mfma_scale_f32_32x32x64_f8f6f4 v[2:17], v[50:57], v[178:185], v[2:17], v234, v234 op_sel_hi:[0,0,0]
	s_waitcnt lgkmcnt(0)
	v_mfma_scale_f32_32x32x64_f8f6f4 v[2:17], v[42:49], v[186:193], v[2:17], v234, v234 op_sel_hi:[0,0,0]
	ds_read_b128 v[146:149], v231 offset:34944
	ds_read_b128 v[150:153], v231 offset:34976
	ds_read_b128 v[154:157], v231 offset:35008
	ds_read_b128 v[158:161], v231 offset:35040
	s_waitcnt lgkmcnt(0)
	v_mfma_scale_f32_32x32x64_f8f6f4 v[146:161], v[18:25], v[162:169], v[146:161], v234, v234 op_sel_hi:[0,0,0]
	v_mfma_scale_f32_32x32x64_f8f6f4 v[146:161], v[130:137], v[170:177], v[146:161], v234, v234 op_sel_hi:[0,0,0]
	v_mfma_scale_f32_32x32x64_f8f6f4 v[146:161], v[122:129], v[178:185], v[146:161], v234, v234 op_sel_hi:[0,0,0]
	v_mfma_scale_f32_32x32x64_f8f6f4 v[146:161], v[138:145], v[186:193], v[146:161], v234, v234 op_sel_hi:[0,0,0]
	s_nop 15
	v_min3_f32 v2, v2, v3, v4
	v_min3_f32 v5, v5, v6, v7
	v_min3_f32 v8, v8, v9, v10
	v_min3_f32 v11, v11, v12, v13
	v_min3_f32 v14, v14, v15, v16
	v_min3_f32 v2, v2, v5, v8
	v_min3_f32 v11, v11, v14, v17
	v_min_f32_e32 v235, v2, v11
	ds_read_b128 v[2:5], v231 offset:35072
	ds_read_b128 v[6:9], v231 offset:35104
	ds_read_b128 v[10:13], v231 offset:35136
	ds_read_b128 v[14:17], v231 offset:35168
	s_waitcnt lgkmcnt(0)
	v_mfma_scale_f32_32x32x64_f8f6f4 v[2:17], v[98:105], v[162:169], v[2:17], v234, v234 op_sel_hi:[0,0,0]
	v_mfma_scale_f32_32x32x64_f8f6f4 v[2:17], v[90:97], v[170:177], v[2:17], v234, v234 op_sel_hi:[0,0,0]
	v_mfma_scale_f32_32x32x64_f8f6f4 v[2:17], v[114:121], v[178:185], v[2:17], v234, v234 op_sel_hi:[0,0,0]
	v_mfma_scale_f32_32x32x64_f8f6f4 v[2:17], v[106:113], v[186:193], v[2:17], v234, v234 op_sel_hi:[0,0,0]
	s_nop 15
	v_min3_f32 v146, v146, v147, v148
	v_min3_f32 v149, v149, v150, v151
	v_min3_f32 v152, v152, v153, v154
	v_min3_f32 v155, v155, v156, v157
	v_min3_f32 v158, v158, v159, v160
	v_min3_f32 v146, v146, v149, v152
	v_min3_f32 v155, v155, v158, v161
	v_min3_f32 v235, v235, v146, v155
	ds_read_b128 v[146:149], v231 offset:35200
	ds_read_b128 v[150:153], v231 offset:35232
	ds_read_b128 v[154:157], v231 offset:35264
	ds_read_b128 v[158:161], v231 offset:35296
	s_waitcnt lgkmcnt(0)
	v_mfma_scale_f32_32x32x64_f8f6f4 v[146:161], v[58:65], v[162:169], v[146:161], v234, v234 op_sel_hi:[0,0,0]
	v_mfma_scale_f32_32x32x64_f8f6f4 v[146:161], v[66:73], v[170:177], v[146:161], v234, v234 op_sel_hi:[0,0,0]
	v_mfma_scale_f32_32x32x64_f8f6f4 v[146:161], v[74:81], v[178:185], v[146:161], v234, v234 op_sel_hi:[0,0,0]
	v_mfma_scale_f32_32x32x64_f8f6f4 v[146:161], v[82:89], v[186:193], v[146:161], v234, v234 op_sel_hi:[0,0,0]
	s_nop 15
	v_min3_f32 v2, v2, v3, v4
	v_min3_f32 v5, v5, v6, v7
	v_min3_f32 v8, v8, v9, v10
	v_min3_f32 v11, v11, v12, v13
	v_min3_f32 v14, v14, v15, v16
	v_min3_f32 v2, v2, v5, v8
	v_min3_f32 v11, v11, v14, v17
	v_min3_f32 v235, v235, v2, v11
	s_nop 15
	s_nop 3
	v_min3_f32 v146, v146, v147, v148
	v_min3_f32 v149, v149, v150, v151
	v_min3_f32 v152, v152, v153, v154
	v_min3_f32 v155, v155, v156, v157
	v_min3_f32 v158, v158, v159, v160
	v_min3_f32 v146, v146, v149, v152
	v_min3_f32 v155, v155, v158, v161
	v_min3_f32 v235, v235, v146, v155
	ds_bpermute_b32 v246, v232, v235
	s_waitcnt lgkmcnt(0)
	v_min_f32_e32 v246, v235, v246
	ds_write_b32 v233, v246 offset:49152
	s_waitcnt vmcnt(0)
	v_mul_f32_e32 v244, v210, v210
	v_mul_f32_e32 v245, v214, v214
	v_cvt_pk_fp8_f32 v240, v210, v211
	v_cvt_pk_fp8_f32 v241, v214, v215
	v_cvt_pk_fp8_f32 v242, v218, v219
	v_cvt_pk_fp8_f32 v243, v222, v223
	v_fmac_f32_e32 v244, v211, v211
	v_fmac_f32_e32 v245, v215, v215
	v_fmac_f32_e32 v244, v212, v212
	v_fmac_f32_e32 v245, v216, v216
	v_fmac_f32_e32 v244, v213, v213
	v_fmac_f32_e32 v245, v217, v217
	v_fmac_f32_e32 v244, v218, v218
	v_fmac_f32_e32 v245, v222, v222
	v_fmac_f32_e32 v244, v219, v219
	v_fmac_f32_e32 v245, v223, v223
	v_fmac_f32_e32 v244, v220, v220
	v_fmac_f32_e32 v245, v224, v224
	v_fmac_f32_e32 v244, v221, v221
	v_fmac_f32_e32 v245, v225, v225
	v_cvt_pk_fp8_f32 v240, v212, v213 op_sel:[0,0,1]
	v_cvt_pk_fp8_f32 v241, v216, v217 op_sel:[0,0,1]
	v_cvt_pk_fp8_f32 v242, v220, v221 op_sel:[0,0,1]
	v_cvt_pk_fp8_f32 v243, v224, v225 op_sel:[0,0,1]
	v_add_f32_e32 v244, v244, v245
	s_nop 0
	ds_write_b128 v228, v[240:243] offset:26112
	ds_write_b32 v229, v244 offset:45056
	s_waitcnt lgkmcnt(0)
	s_barrier
	ds_read_b128 v[162:165], v230 offset:26112
	ds_read_b128 v[166:169], v230 offset:26128
	ds_read_b128 v[2:5], v231 offset:34816
	ds_read_b128 v[6:9], v231 offset:34848
	ds_read_b128 v[10:13], v231 offset:34880
	ds_read_b128 v[14:17], v231 offset:34912
	ds_read_b128 v[170:173], v230 offset:26176
	ds_read_b128 v[174:177], v230 offset:26192
	ds_read_b128 v[178:181], v230 offset:26240
	ds_read_b128 v[182:185], v230 offset:26256
	ds_read_b128 v[186:189], v230 offset:26304
	ds_read_b128 v[190:193], v230 offset:26320
	s_waitcnt lgkmcnt(6)
	v_mfma_scale_f32_32x32x64_f8f6f4 v[2:17], v[34:41], v[162:169], v[2:17], v234, v234 op_sel_hi:[0,0,0]
	s_waitcnt lgkmcnt(4)
	v_mfma_scale_f32_32x32x64_f8f6f4 v[2:17], v[26:33], v[170:177], v[2:17], v234, v234 op_sel_hi:[0,0,0]
	s_waitcnt lgkmcnt(2)
	v_mfma_scale_f32_32x32x64_f8f6f4 v[2:17], v[50:57], v[178:185], v[2:17], v234, v234 op_sel_hi:[0,0,0]
	s_waitcnt lgkmcnt(0)
	v_mfma_scale_f32_32x32x64_f8f6f4 v[2:17], v[42:49], v[186:193], v[2:17], v234, v234 op_sel_hi:[0,0,0]
	ds_read_b128 v[146:149], v231 offset:34944
	ds_read_b128 v[150:153], v231 offset:34976
	ds_read_b128 v[154:157], v231 offset:35008
	ds_read_b128 v[158:161], v231 offset:35040
	s_waitcnt lgkmcnt(0)
	v_mfma_scale_f32_32x32x64_f8f6f4 v[146:161], v[18:25], v[162:169], v[146:161], v234, v234 op_sel_hi:[0,0,0]
	v_mfma_scale_f32_32x32x64_f8f6f4 v[146:161], v[130:137], v[170:177], v[146:161], v234, v234 op_sel_hi:[0,0,0]
	v_mfma_scale_f32_32x32x64_f8f6f4 v[146:161], v[122:129], v[178:185], v[146:161], v234, v234 op_sel_hi:[0,0,0]
	v_mfma_scale_f32_32x32x64_f8f6f4 v[146:161], v[138:145], v[186:193], v[146:161], v234, v234 op_sel_hi:[0,0,0]
	s_nop 15
	v_min3_f32 v2, v2, v3, v4
	v_min3_f32 v5, v5, v6, v7
	v_min3_f32 v8, v8, v9, v10
	v_min3_f32 v11, v11, v12, v13
	v_min3_f32 v14, v14, v15, v16
	v_min3_f32 v2, v2, v5, v8
	v_min3_f32 v11, v11, v14, v17
	v_min_f32_e32 v235, v2, v11
	ds_read_b128 v[2:5], v231 offset:35072
	ds_read_b128 v[6:9], v231 offset:35104
	ds_read_b128 v[10:13], v231 offset:35136
	ds_read_b128 v[14:17], v231 offset:35168
	s_waitcnt lgkmcnt(0)
	v_mfma_scale_f32_32x32x64_f8f6f4 v[2:17], v[98:105], v[162:169], v[2:17], v234, v234 op_sel_hi:[0,0,0]
	v_mfma_scale_f32_32x32x64_f8f6f4 v[2:17], v[90:97], v[170:177], v[2:17], v234, v234 op_sel_hi:[0,0,0]
	v_mfma_scale_f32_32x32x64_f8f6f4 v[2:17], v[114:121], v[178:185], v[2:17], v234, v234 op_sel_hi:[0,0,0]
	v_mfma_scale_f32_32x32x64_f8f6f4 v[2:17], v[106:113], v[186:193], v[2:17], v234, v234 op_sel_hi:[0,0,0]
	s_nop 15
	v_min3_f32 v146, v146, v147, v148
	v_min3_f32 v149, v149, v150, v151
	v_min3_f32 v152, v152, v153, v154
	v_min3_f32 v155, v155, v156, v157
	v_min3_f32 v158, v158, v159, v160
	v_min3_f32 v146, v146, v149, v152
	v_min3_f32 v155, v155, v158, v161
	v_min3_f32 v235, v235, v146, v155
	ds_read_b128 v[146:149], v231 offset:35200
	ds_read_b128 v[150:153], v231 offset:35232
	ds_read_b128 v[154:157], v231 offset:35264
	ds_read_b128 v[158:161], v231 offset:35296
	s_waitcnt lgkmcnt(0)
	v_mfma_scale_f32_32x32x64_f8f6f4 v[146:161], v[58:65], v[162:169], v[146:161], v234, v234 op_sel_hi:[0,0,0]
	v_mfma_scale_f32_32x32x64_f8f6f4 v[146:161], v[66:73], v[170:177], v[146:161], v234, v234 op_sel_hi:[0,0,0]
	v_mfma_scale_f32_32x32x64_f8f6f4 v[146:161], v[74:81], v[178:185], v[146:161], v234, v234 op_sel_hi:[0,0,0]
	v_mfma_scale_f32_32x32x64_f8f6f4 v[146:161], v[82:89], v[186:193], v[146:161], v234, v234 op_sel_hi:[0,0,0]
	s_nop 15
	v_min3_f32 v2, v2, v3, v4
	v_min3_f32 v5, v5, v6, v7
	v_min3_f32 v8, v8, v9, v10
	v_min3_f32 v11, v11, v12, v13
	v_min3_f32 v14, v14, v15, v16
	v_min3_f32 v2, v2, v5, v8
	v_min3_f32 v11, v11, v14, v17
	v_min3_f32 v235, v235, v2, v11
	s_nop 15
	s_nop 3
	v_min3_f32 v146, v146, v147, v148
	v_min3_f32 v149, v149, v150, v151
	v_min3_f32 v152, v152, v153, v154
	v_min3_f32 v155, v155, v156, v157
	v_min3_f32 v158, v158, v159, v160
	v_min3_f32 v146, v146, v149, v152
	v_min3_f32 v155, v155, v158, v161
	v_min3_f32 v235, v235, v146, v155
	ds_bpermute_b32 v246, v232, v235
	s_waitcnt lgkmcnt(0)
	v_min_f32_e32 v246, v235, v246
	ds_write_b32 v233, v246 offset:50176
	s_waitcnt lgkmcnt(0)
	s_barrier
	v_readfirstlane_b32 s2, v1
	s_cmp_gt_u32 s2, 1
	s_cbranch_scc1 .Lmain_idle
	v_and_b32_e32 v2, 31, v0
	v_lshlrev_b32_e32 v3, 5, v0
	v_and_b32_e32 v3, 0xc00, v3
	v_lshl_or_b32 v8, v2, 2, v3
	v_add_u32_e32 v8, 0xb800, v8
	v_lshlrev_b32_e32 v14, 6, v0
	ds_read2_b32 v[2:3], v8 offset1:32
	ds_read2_b32 v[4:5], v8 offset0:64 offset1:96
	ds_read2_b32 v[6:7], v8 offset0:128 offset1:160
	ds_read2_b32 v[10:11], v8 offset0:192 offset1:224
	ds_read_b128 v[20:23], v14 offset:38912
	ds_read_b128 v[24:27], v14 offset:38928
	ds_read_b128 v[28:31], v14 offset:38944
	ds_read_b128 v[32:35], v14 offset:38960
	s_mov_b32 s8, 0xf800000
	s_waitcnt lgkmcnt(4)
	v_min3_f32 v2, v2, v3, v4
	v_min3_f32 v5, v5, v6, v7
	v_min3_f32 v2, v2, v10, v11
	v_min_f32_e32 v2, v2, v5
	s_waitcnt lgkmcnt(0)
	v_add_f32_e32 v20, v20, v21
	v_add_f32_e32 v22, v22, v23
	v_add_f32_e32 v24, v24, v25
	v_add_f32_e32 v26, v26, v27
	v_add_f32_e32 v28, v28, v29
	v_add_f32_e32 v30, v30, v31
	v_add_f32_e32 v32, v32, v33
	v_add_f32_e32 v34, v34, v35
	v_add_f32_e32 v20, v20, v22
	v_add_f32_e32 v24, v24, v26
	v_add_f32_e32 v28, v28, v30
	v_add_f32_e32 v32, v32, v34
	v_add_f32_e32 v20, v20, v24
	v_add_f32_e32 v28, v28, v32
	v_add_f32_e32 v20, v20, v28
	v_add_f32_e32 v2, v2, v20
	v_max_f32_e32 v2, 0, v2
	v_mul_f32_e32 v3, 0x4f800000, v2
	v_cmp_gt_f32_e32 vcc, s8, v2
	s_nop 1
	v_cndmask_b32_e32 v2, v2, v3, vcc
	v_sqrt_f32_e32 v3, v2
	s_nop 0
	v_add_u32_e32 v4, -1, v3
	v_fma_f32 v5, -v4, v3, v2
	v_cmp_ge_f32_e64 s[10:11], 0, v5
	v_add_u32_e32 v5, 1, v3
	s_nop 0
	v_cndmask_b32_e64 v4, v3, v4, s[10:11]
	v_fma_f32 v3, -v5, v3, v2
	v_cmp_lt_f32_e64 s[10:11], 0, v3
	s_nop 1
	v_cndmask_b32_e64 v3, v4, v5, s[10:11]
	v_mul_f32_e32 v4, 0x37800000, v3
	v_cndmask_b32_e32 v3, v3, v4, vcc
	v_mov_b32_e32 v4, 0x260
	v_cmp_class_f32_e32 vcc, v2, v4
	s_nop 1
	v_cndmask_b32_e32 v2, v3, v2, vcc
	s_nop 1
	v_add_f32_dpp v3, v2, v2 quad_perm:[1,0,3,2] row_mask:0xf bank_mask:0xf
	s_nop 1
	v_add_f32_dpp v4, v3, v3 quad_perm:[2,3,0,1] row_mask:0xf bank_mask:0xf
	s_nop 1
	v_add_f32_dpp v5, v4, v4 row_half_mirror row_mask:0xf bank_mask:0xf
	s_nop 1
	v_add_f32_dpp v6, v5, v5 row_mirror row_mask:0xf bank_mask:0xf
	s_nop 1
	v_readlane_b32 s12, v6, 0
	v_readlane_b32 s13, v6, 16
	v_readlane_b32 s14, v6, 32
	v_readlane_b32 s15, v6, 48
	s_nop 3
	v_mov_b32_e32 v7, s12
	v_add_f32_e32 v7, s13, v7
	v_mov_b32_e32 v9, s14
	v_add_f32_e32 v9, s15, v9
	v_add_f32_e32 v7, v7, v9
	v_mov_b32_e32 v4, 0
	s_cmp_eq_u32 s2, 1
	s_cbranch_scc0 .Lmain_w0
	ds_write_b32 v4, v7 offset:51204
	s_waitcnt lgkmcnt(0)
.Lmain_idle:
	s_barrier
	s_endpgm
.Lmain_w0:
	s_load_dwordx2 s[0:1], s[0:1], 0x18
	s_lshr_b32 s2, s30, 4
	s_lshl_b32 s2, s2, 7
	s_add_u32 s2, s2, 0x300000
	s_add_u32 s6, s6, s2
	s_addc_u32 s7, s7, 0
	s_mov_b32 s4, 0
	s_mov_b32 s5, 0x41d00000
	s_mov_b32 s8, 0
	s_mov_b32 s9, 0x420e0000
	s_barrier
	ds_read_b32 v3, v4 offset:51204
	s_mov_b64 exec, 1
	s_waitcnt lgkmcnt(0)
	v_add_f32_e32 v0, v7, v3
	v_cvt_f64_f32_e32 v[6:7], v0
	v_add_f64 v[8:9], v[6:7], s[4:5]
	global_atomic_add_f64 v[10:11], v4, v[8:9], s[6:7] sc0
	s_waitcnt vmcnt(0)
	v_cmp_le_f64_e32 vcc, s[8:9], v[10:11]
	s_and_saveexec_b64 s[2:3], vcc
	s_cbranch_execz .Lmain_end
	v_add_f64 v[10:11], v[10:11], -s[8:9]
	v_add_f64 v[10:11], v[10:11], v[6:7]
	v_cvt_f32_f64_e32 v0, v[10:11]
	v_mul_f32_e32 v0, 0x38000000, v0
	global_atomic_add_f32 v4, v0, s[0:1]

	.amdhsa_kernel _Z11center_mainPKfPKcS0_Pf
		.amdhsa_group_segment_fixed_size 51232
		.amdhsa_private_segment_fixed_size 0
		.amdhsa_kernarg_size 32
		.amdhsa_user_sgpr_count 2
		.amdhsa_user_sgpr_dispatch_ptr 0
		.amdhsa_user_sgpr_queue_ptr 0
		.amdhsa_user_sgpr_kernarg_segment_ptr 1
		.amdhsa_user_sgpr_dispatch_id 0
		.amdhsa_user_sgpr_kernarg_preload_length 0
		.amdhsa_user_sgpr_kernarg_preload_offset 0
		.amdhsa_user_sgpr_private_segment_size 0
		.amdhsa_uses_dynamic_stack 0
		.amdhsa_enable_private_segment 0
		.amdhsa_system_sgpr_workgroup_id_x 1
		.amdhsa_system_sgpr_workgroup_id_y 0
		.amdhsa_system_sgpr_workgroup_id_z 0
		.amdhsa_system_sgpr_workgroup_info 0
		.amdhsa_system_vgpr_workitem_id 0
		.amdhsa_next_free_vgpr 248
		.amdhsa_next_free_sgpr 91
		.amdhsa_accum_offset 248
		.amdhsa_reserve_vcc 1
		.amdhsa_float_round_mode_32 0
		.amdhsa_float_round_mode_16_64 0
		.amdhsa_float_denorm_mode_32 3
		.amdhsa_float_denorm_mode_16_64 3
		.amdhsa_dx10_clamp 1
		.amdhsa_ieee_mode 1
		.amdhsa_fp16_overflow 0
		.amdhsa_tg_split 0
		.amdhsa_exception_fp_ieee_invalid_op 0
		.amdhsa_exception_fp_denorm_src 0
		.amdhsa_exception_fp_ieee_div_zero 0
		.amdhsa_exception_fp_ieee_overflow 0
		.amdhsa_exception_fp_ieee_underflow 0
		.amdhsa_exception_fp_ieee_inexact 0
		.amdhsa_exception_int_div_zero 0
	.end_amdhsa_kernel

.Lfunc_end1:
	.size	_Z11center_mainPKfPKcS0_Pf, .Lfunc_end1-_Z11center_mainPKfPKcS0_Pf
	.set _Z11center_mainPKfPKcS0_Pf.num_vgpr, 248
	.set _Z11center_mainPKfPKcS0_Pf.num_agpr, 0
	.set _Z11center_mainPKfPKcS0_Pf.numbered_sgpr, 12
	.set _Z11center_mainPKfPKcS0_Pf.num_named_barrier, 0
	.set _Z11center_mainPKfPKcS0_Pf.private_seg_size, 0
	.set _Z11center_mainPKfPKcS0_Pf.uses_vcc, 1
	.set _Z11center_mainPKfPKcS0_Pf.uses_flat_scratch, 0
	.set _Z11center_mainPKfPKcS0_Pf.has_dyn_sized_stack, 0
	.set _Z11center_mainPKfPKcS0_Pf.has_recursion, 0
	.set _Z11center_mainPKfPKcS0_Pf.has_indirect_call, 0

amdhsa.kernels:
  - .agpr_count:     0
    .args:
      - .actual_access:  read_only
        .address_space:  global
        .offset:         0
        .size:           8
        .value_kind:     global_buffer
      - .actual_access:  write_only
        .address_space:  global
        .offset:         8
        .size:           8
        .value_kind:     global_buffer
      - .actual_access:  write_only
        .address_space:  global
        .offset:         16
        .size:           8
        .value_kind:     global_buffer
      - .actual_access:  write_only
        .address_space:  global
        .offset:         24
        .size:           8
        .value_kind:     global_buffer
    .group_segment_fixed_size: 8704
    .kernarg_segment_align: 8
    .kernarg_segment_size: 32
    .language:       OpenCL C
    .language_version:
      - 2
      - 0
    .max_flat_workgroup_size: 64
    .name:           _Z11center_prepPKfPcPfS2_
    .private_segment_fixed_size: 0
    .sgpr_count:     18
    .sgpr_spill_count: 0
    .symbol:         _Z11center_prepPKfPcPfS2_.kd
    .uniform_work_group_size: 1
    .uses_dynamic_stack: false
    .vgpr_count:     164
    .vgpr_spill_count: 0
    .wavefront_size: 64
  - .agpr_count:     0
    .args:
      - .actual_access:  read_only
        .address_space:  global
        .offset:         0
        .size:           8
        .value_kind:     global_buffer
      - .actual_access:  read_only
        .address_space:  global
        .offset:         8
        .size:           8
        .value_kind:     global_buffer
      - .actual_access:  read_only
        .address_space:  global
        .offset:         16
        .size:           8
        .value_kind:     global_buffer
      - .address_space:  global
        .offset:         24
        .size:           8
        .value_kind:     global_buffer
    .group_segment_fixed_size: 51232
    .kernarg_segment_align: 8
    .kernarg_segment_size: 32
    .language:       OpenCL C
    .language_version:
      - 2
      - 0
    .max_flat_workgroup_size: 512
    .name:           _Z11center_mainPKfPKcS0_Pf
    .private_segment_fixed_size: 0
    .sgpr_count:     18
    .sgpr_spill_count: 0
    .symbol:         _Z11center_mainPKfPKcS0_Pf.kd
    .uniform_work_group_size: 1
    .uses_dynamic_stack: false
    .vgpr_count:     248
    .vgpr_spill_count: 0
    .wavefront_size: 64
